# v42 + tier-1 flag ballot trimmed (s_and_b64 + scc branch instead of cndmask/cmp_ne/s_mov)
# speedup vs baseline: 1.0098x; 1.0038x over previous
.LBB1_10:
	s_or_b64 exec, exec, s[0:1]
	v_add_f32_e32 v6, v6, v7
	v_add_f32_e32 v7, v8, v9
	v_add_f32_e32 v2, v2, v3
	v_add_f32_e32 v3, v4, v5
	v_add_f32_e32 v6, v6, v7
	v_add_f32_e32 v2, v2, v3
	v_add_f32_e32 v2, v6, v2
	v_mul_f32_e32 v2, 0x36800000, v2
	s_mov_b32 s3, 0xf800000
	v_mul_f32_e32 v3, 0x4f800000, v2
	v_cmp_gt_f32_e32 vcc, s3, v2
	v_add_f32_e32 v4, v133, v134
	v_add_f32_e32 v5, v135, v136
	v_cndmask_b32_e32 v2, v2, v3, vcc
	v_sqrt_f32_e32 v3, v2
	v_cndmask_b32_e64 v4, v5, v4, s[4:5]
	v_mov_b32_e32 v23, 0x260
	v_and_b32_e32 v17, 0x7fffffff, v12
	v_add_u32_e32 v5, -1, v3
	v_fma_f32 v6, -v5, v3, v2
	v_cmp_ge_f32_e64 s[0:1], 0, v6
	v_add_u32_e32 v6, 1, v3
	v_and_b32_e32 v22, 0x3ff, v12
	v_cndmask_b32_e64 v5, v3, v5, s[0:1]
	v_fma_f32 v3, -v6, v3, v2
	v_cmp_lt_f32_e64 s[0:1], 0, v3
	s_brev_b32 s33, -2
	s_nop 0
	v_cndmask_b32_e64 v3, v5, v6, s[0:1]
	v_mul_f32_e32 v5, 0x37800000, v3
	v_cndmask_b32_e32 v3, v3, v5, vcc
	v_mul_f32_e32 v5, 0x4f800000, v4
	v_cmp_gt_f32_e32 vcc, s3, v4
	v_cmp_class_f32_e64 s[0:1], v2, v23
	s_nop 0
	v_cndmask_b32_e32 v4, v4, v5, vcc
	v_sqrt_f32_e32 v5, v4
	v_cndmask_b32_e64 v3, v3, v2, s[0:1]
	v_cndmask_b32_e64 v2, v16, v13, s[4:5]
	v_add_u32_e32 v6, -1, v5
	v_fma_f32 v7, -v6, v5, v4
	v_cmp_ge_f32_e64 s[0:1], 0, v7
	v_add_u32_e32 v7, 1, v5
	s_nop 0
	v_cndmask_b32_e64 v6, v5, v6, s[0:1]
	v_fma_f32 v5, -v7, v5, v4
	v_cmp_lt_f32_e64 s[0:1], 0, v5
	s_nop 1
	v_cndmask_b32_e64 v5, v6, v7, s[0:1]
	v_mul_f32_e32 v6, 0x37800000, v5
	v_cndmask_b32_e32 v5, v5, v6, vcc
	v_cmp_class_f32_e32 vcc, v4, v23
	s_mov_b32 s0, 0x3b51b717
	s_mov_b32 s1, 0x39800000
	v_cndmask_b32_e32 v4, v5, v4, vcc
	v_mul_f32_e32 v16, v3, v4
	v_pk_mul_f32 v[4:5], v[16:17], s[0:1]
	s_nop 0
	v_add_f32_e32 v3, v4, v5
	v_add_f32_e32 v3, 0x358637bd, v3
	v_sub_f32_e32 v4, v2, v12
	v_cmp_lt_f32_e32 vcc, v4, v3
	s_and_b64 s[8:9], s[6:7], vcc
	s_cbranch_scc0 .LBB1_51
	v_cndmask_b32_e64 v4, v11, v10, s[4:5]
	v_and_b32_e32 v17, 0x3ff, v2
	v_and_b32_e32 v2, 0x3ff, v4
	v_sub_f32_e32 v4, v4, v12
	v_cmp_lt_f32_e32 vcc, v4, v3
	v_add_u32_e32 v6, 0x19060, v130
	v_mov_b32_e32 v131, 0
	v_cndmask_b32_e32 v24, -1, v2, vcc
	v_add_u32_e32 v2, 0x19460, v130
	ds_read_b128 v[2:5], v2
	ds_read_b128 v[6:9], v6
	v_lshl_add_u64 v[18:19], s[20:21], 0, v[130:131]
	v_lshl_add_u64 v[20:21], s[36:37], 0, v[130:131]
	v_mov_b32_e32 v25, 0x3727c5ac
	s_mov_b32 s5, 0
	s_mov_b32 s34, 0x378e98ab
	s_mov_b32 s35, 0x3b7cd369
	s_mov_b32 s36, 0xbcc618b2
	s_mov_b32 s37, 0x3dda74e4
	s_mov_b32 s40, 0x3f228afd
	s_mov_b32 s41, 0x3e03c728
	s_mov_b32 s42, 0xbfb8aa3b
	s_mov_b32 s43, 0x42ce8ed0
	s_mov_b32 s44, 0xc2b17218
	v_mov_b32_e32 v26, 0x3ba10414
	v_mov_b32_e32 v27, 0x33d6bf95
	v_mov_b32_e32 v28, 0x3851b717
	v_mov_b32_e32 v29, 0xb9c68948
	v_mov_b32_e32 v30, 0x7f800000
	s_branch .LBB1_15
